# P11: xor-8/4/2/1 steps of the per-token wave sum as DPP moves (bit-identical)
# speedup vs baseline: 1.0006x; 1.0006x over previous
.LBB0_1168:
	s_add_u32 s14, s76, s6
	v_lshl_add_u64 v[4:5], s[76:77], 0, v[40:41]
	s_addc_u32 s15, s77, s7
	v_add_co_u32_e32 v72, vcc, s1, v4
	global_load_dwordx4 v[0:3], v[12:13], off
	s_nop 0
	v_addc_co_u32_e32 v73, vcc, 0, v5, vcc
	global_load_dwordx4 v[60:63], v48, s[14:15]
	global_load_dwordx4 v[64:67], v49, s[14:15]
	global_load_dwordx2 v[74:75], v[72:73], off offset:512
	global_load_dwordx2 v[76:77], v[72:73], off offset:1024
	global_load_dwordx2 v[78:79], v[72:73], off offset:1536
	global_load_dwordx2 v[80:81], v[72:73], off offset:2048
	global_load_dwordx2 v[82:83], v[72:73], off offset:2560
	global_load_dwordx2 v[84:85], v[72:73], off offset:3072
	s_ashr_i32 s16, s0, 13
	s_mul_i32 s14, s16, 0x3000
	s_ashr_i32 s15, s14, 31
	s_lshl_b64 s[14:15], s[14:15], 2
	s_add_u32 s14, s76, s14
	s_addc_u32 s15, s77, s15
	s_add_u32 s14, s14, 0xda000
	s_addc_u32 s15, s15, 0
	global_load_dwordx4 v[68:71], v50, s[14:15]
	global_load_dwordx2 v[86:87], v[72:73], off
	global_load_dwordx4 v[8:11], v52, s[14:15]
	global_load_dwordx4 v[4:7], v56, s[14:15]
	s_add_i32 s0, s0, s4
	s_add_u32 s6, s6, s8
	s_addc_u32 s7, s7, s9
	v_lshl_add_u64 v[40:41], v[40:41], 0, s[12:13]
	s_cmpk_lt_i32 s0, 0x4000
	s_waitcnt vmcnt(11)
	v_mul_f32_e32 v88, 0x3d800000, v60
	v_mul_f32_e32 v90, 0x3d800000, v61
	s_waitcnt vmcnt(10)
	v_ashrrev_i32_e32 v61, 31, v64
	v_mov_b32_e32 v60, v64
	v_mul_f32_e32 v92, 0x3d800000, v62
	v_mul_f32_e32 v94, 0x3d800000, v63
	v_ashrrev_i32_e32 v63, 31, v65
	v_mov_b32_e32 v62, v65
	v_ashrrev_i32_e32 v65, 31, v66
	v_mov_b32_e32 v64, v66
	v_ashrrev_i32_e32 v97, 31, v67
	v_mov_b32_e32 v96, v67
	v_lshlrev_b64 v[60:61], 11, v[60:61]
	s_waitcnt vmcnt(9)
	v_lshlrev_b32_e32 v98, 16, v74
	v_and_b32_e32 v99, 0xffff0000, v74
	v_lshlrev_b32_e32 v100, 16, v75
	v_and_b32_e32 v101, 0xffff0000, v75
	v_lshlrev_b64 v[62:63], 11, v[62:63]
	v_lshlrev_b64 v[66:67], 11, v[96:97]
	v_lshlrev_b64 v[64:65], 11, v[64:65]
	v_lshl_add_u64 v[74:75], v[14:15], 0, v[60:61]
	s_waitcnt vmcnt(8)
	v_lshlrev_b32_e32 v102, 16, v76
	v_and_b32_e32 v103, 0xffff0000, v76
	v_lshlrev_b32_e32 v104, 16, v77
	v_and_b32_e32 v105, 0xffff0000, v77
	s_waitcnt vmcnt(7)
	v_lshlrev_b32_e32 v106, 16, v78
	v_and_b32_e32 v107, 0xffff0000, v78
	v_lshlrev_b32_e32 v108, 16, v79
	v_and_b32_e32 v109, 0xffff0000, v79
	s_waitcnt vmcnt(6)
	v_lshlrev_b32_e32 v110, 16, v80
	v_and_b32_e32 v111, 0xffff0000, v80
	v_lshlrev_b32_e32 v112, 16, v81
	v_and_b32_e32 v113, 0xffff0000, v81
	v_lshl_add_u64 v[76:77], v[14:15], 0, v[62:63]
	v_lshl_add_u64 v[78:79], v[14:15], 0, v[64:65]
	v_lshl_add_u64 v[80:81], v[14:15], 0, v[66:67]
	global_load_dword v59, v[74:75], off
	global_load_dword v89, v[76:77], off
	global_load_dword v91, v[78:79], off
	global_load_dword v93, v[80:81], off
	v_lshl_add_u64 v[60:61], s[2:3], 0, v[60:61]
	v_lshl_add_u64 v[62:63], s[2:3], 0, v[62:63]
	v_lshl_add_u64 v[64:65], s[2:3], 0, v[64:65]
	v_lshl_add_u64 v[66:67], s[2:3], 0, v[66:67]
	v_lshl_add_u64 v[74:75], v[60:61], 0, v[16:17]
	v_lshl_add_u64 v[76:77], v[62:63], 0, v[16:17]
	v_lshl_add_u64 v[78:79], v[64:65], 0, v[16:17]
	v_lshl_add_u64 v[80:81], v[66:67], 0, v[16:17]
	v_lshl_add_u64 v[96:97], v[60:61], 0, v[18:19]
	v_lshl_add_u64 v[114:115], v[62:63], 0, v[18:19]
	v_lshl_add_u64 v[116:117], v[64:65], 0, v[18:19]
	v_lshl_add_u64 v[118:119], v[66:67], 0, v[18:19]
	v_lshl_add_u64 v[120:121], v[60:61], 0, v[20:21]
	v_lshl_add_u64 v[122:123], v[62:63], 0, v[20:21]
	v_lshl_add_u64 v[124:125], v[64:65], 0, v[20:21]
	v_lshl_add_u64 v[126:127], v[66:67], 0, v[20:21]
	v_lshl_add_u64 v[128:129], v[60:61], 0, v[22:23]
	v_lshl_add_u64 v[130:131], v[62:63], 0, v[22:23]
	v_lshl_add_u64 v[132:133], v[64:65], 0, v[22:23]
	v_lshl_add_u64 v[134:135], v[66:67], 0, v[22:23]
	v_lshl_add_u64 v[136:137], v[60:61], 0, v[24:25]
	v_lshl_add_u64 v[138:139], v[62:63], 0, v[24:25]
	v_lshl_add_u64 v[140:141], v[64:65], 0, v[24:25]
	v_lshl_add_u64 v[142:143], v[66:67], 0, v[24:25]
	v_lshl_add_u64 v[144:145], v[60:61], 0, v[26:27]
	v_lshl_add_u64 v[146:147], v[62:63], 0, v[26:27]
	v_lshl_add_u64 v[148:149], v[64:65], 0, v[26:27]
	v_lshl_add_u64 v[150:151], v[66:67], 0, v[26:27]
	v_lshl_add_u64 v[60:61], v[60:61], 0, v[28:29]
	v_lshl_add_u64 v[62:63], v[62:63], 0, v[28:29]
	v_lshl_add_u64 v[64:65], v[64:65], 0, v[28:29]
	v_lshl_add_u64 v[66:67], v[66:67], 0, v[28:29]
	global_load_dword v95, v[74:75], off
	global_load_dword v152, v[76:77], off
	global_load_dword v153, v[78:79], off
	global_load_dword v154, v[80:81], off
	global_load_dword v156, v[96:97], off
	global_load_dword v160, v[114:115], off
	global_load_dword v164, v[116:117], off
	global_load_dword v168, v[118:119], off
	global_load_dword v172, v[120:121], off
	global_load_dword v176, v[122:123], off
	global_load_dword v180, v[124:125], off
	global_load_dword v184, v[126:127], off
	global_load_dword v188, v[128:129], off
	global_load_dword v192, v[130:131], off
	global_load_dword v196, v[132:133], off
	global_load_dword v200, v[134:135], off
	global_load_dword v204, v[136:137], off
	global_load_dword v208, v[138:139], off
	global_load_dword v212, v[140:141], off
	global_load_dword v216, v[142:143], off
	global_load_dword v220, v[144:145], off
	global_load_dword v224, v[146:147], off
	global_load_dword v228, v[148:149], off
	global_load_dword v232, v[150:151], off
	global_load_dword v236, v[60:61], off
	global_load_dword v240, v[62:63], off
	global_load_dword v244, v[64:65], off
	s_nop 0
	global_load_dwordx4 v[60:63], v53, s[14:15]
	global_load_dword v250, v[66:67], off
	global_load_dwordx2 v[96:97], v[72:73], off offset:3584
	s_nop 0
	global_load_dwordx4 v[64:67], v54, s[14:15]
	global_load_dwordx4 v[72:75], v51, s[14:15]
	global_load_dwordx4 v[76:79], v55, s[14:15]
	s_waitcnt vmcnt(42)
	v_lshlrev_b32_e32 v114, 16, v82
	v_and_b32_e32 v115, 0xffff0000, v82
	v_lshlrev_b32_e32 v116, 16, v83
	v_and_b32_e32 v117, 0xffff0000, v83
	global_load_dwordx4 v[80:83], v57, s[14:15]
	s_waitcnt vmcnt(40)
	v_lshlrev_b32_e32 v120, 16, v86
	v_and_b32_e32 v121, 0xffff0000, v86
	v_lshlrev_b32_e32 v86, 16, v87
	v_and_b32_e32 v87, 0xffff0000, v87
	v_lshlrev_b32_e32 v118, 16, v84
	v_and_b32_e32 v119, 0xffff0000, v84
	v_lshlrev_b32_e32 v84, 16, v85
	v_and_b32_e32 v85, 0xffff0000, v85
	s_waitcnt vmcnt(37)
	v_cvt_pk_f32_fp8_sdwa v[124:125], v59 src0_sel:WORD_1
	v_cvt_pk_f32_fp8_e32 v[122:123], v59
	s_waitcnt vmcnt(36)
	v_cvt_pk_f32_fp8_sdwa v[128:129], v89 src0_sel:WORD_1
	s_waitcnt vmcnt(33)
	v_cvt_pk_f32_fp8_e32 v[138:139], v95
	v_cvt_pk_f32_fp8_e32 v[126:127], v89
	v_cvt_pk_f32_fp8_sdwa v[132:133], v91 src0_sel:WORD_1
	v_cvt_pk_f32_fp8_sdwa v[140:141], v95 src0_sel:WORD_1
	s_waitcnt vmcnt(32)
	v_cvt_pk_f32_fp8_e32 v[142:143], v152
	v_cvt_pk_f32_fp8_sdwa v[144:145], v152 src0_sel:WORD_1
	s_waitcnt vmcnt(31)
	v_cvt_pk_f32_fp8_e32 v[146:147], v153
	v_cvt_pk_f32_fp8_sdwa v[148:149], v153 src0_sel:WORD_1
	s_waitcnt vmcnt(30)
	v_cvt_pk_f32_fp8_e32 v[150:151], v154
	v_cvt_pk_f32_fp8_sdwa v[152:153], v154 src0_sel:WORD_1
	s_waitcnt vmcnt(29)
	v_cvt_pk_f32_fp8_e32 v[154:155], v156
	v_cvt_pk_f32_fp8_e32 v[130:131], v91
	v_cvt_pk_f32_fp8_sdwa v[136:137], v93 src0_sel:WORD_1
	v_cvt_pk_f32_fp8_sdwa v[156:157], v156 src0_sel:WORD_1
	s_waitcnt vmcnt(28)
	v_cvt_pk_f32_fp8_e32 v[158:159], v160
	s_waitcnt vmcnt(25)
	v_cvt_pk_f32_fp8_e32 v[170:171], v172
	v_cvt_pk_f32_fp8_sdwa v[172:173], v172 src0_sel:WORD_1
	s_waitcnt vmcnt(21)
	v_cvt_pk_f32_fp8_e32 v[186:187], v188
	v_cvt_pk_f32_fp8_sdwa v[188:189], v188 src0_sel:WORD_1
	s_waitcnt vmcnt(17)
	v_cvt_pk_f32_fp8_e32 v[202:203], v204
	v_cvt_pk_f32_fp8_sdwa v[204:205], v204 src0_sel:WORD_1
	s_waitcnt vmcnt(13)
	v_cvt_pk_f32_fp8_e32 v[218:219], v220
	v_cvt_pk_f32_fp8_sdwa v[220:221], v220 src0_sel:WORD_1
	s_waitcnt vmcnt(9)
	v_cvt_pk_f32_fp8_e32 v[234:235], v236
	v_cvt_pk_f32_fp8_sdwa v[236:237], v236 src0_sel:WORD_1
	v_cvt_pk_f32_fp8_e32 v[134:135], v93
	v_cvt_pk_f32_fp8_sdwa v[160:161], v160 src0_sel:WORD_1
	v_cvt_pk_f32_fp8_e32 v[162:163], v164
	v_cvt_pk_f32_fp8_e32 v[174:175], v176
	v_cvt_pk_f32_fp8_sdwa v[176:177], v176 src0_sel:WORD_1
	v_cvt_pk_f32_fp8_e32 v[190:191], v192
	v_cvt_pk_f32_fp8_sdwa v[192:193], v192 src0_sel:WORD_1
	v_cvt_pk_f32_fp8_e32 v[206:207], v208
	v_cvt_pk_f32_fp8_sdwa v[208:209], v208 src0_sel:WORD_1
	v_cvt_pk_f32_fp8_e32 v[222:223], v224
	v_cvt_pk_f32_fp8_sdwa v[224:225], v224 src0_sel:WORD_1
	s_waitcnt vmcnt(8)
	v_cvt_pk_f32_fp8_e32 v[238:239], v240
	v_cvt_pk_f32_fp8_sdwa v[240:241], v240 src0_sel:WORD_1
	v_pk_fma_f32 v[124:125], v[88:89], v[124:125], 0 op_sel_hi:[0,1,0]
	v_cvt_pk_f32_fp8_sdwa v[164:165], v164 src0_sel:WORD_1
	v_cvt_pk_f32_fp8_e32 v[166:167], v168
	v_cvt_pk_f32_fp8_e32 v[178:179], v180
	v_cvt_pk_f32_fp8_sdwa v[180:181], v180 src0_sel:WORD_1
	v_cvt_pk_f32_fp8_e32 v[194:195], v196
	v_cvt_pk_f32_fp8_sdwa v[196:197], v196 src0_sel:WORD_1
	v_cvt_pk_f32_fp8_e32 v[210:211], v212
	v_cvt_pk_f32_fp8_sdwa v[212:213], v212 src0_sel:WORD_1
	v_cvt_pk_f32_fp8_e32 v[226:227], v228
	v_cvt_pk_f32_fp8_sdwa v[228:229], v228 src0_sel:WORD_1
	s_waitcnt vmcnt(7)
	v_cvt_pk_f32_fp8_e32 v[242:243], v244
	v_cvt_pk_f32_fp8_sdwa v[244:245], v244 src0_sel:WORD_1
	v_pk_fma_f32 v[122:123], v[88:89], v[122:123], 0 op_sel_hi:[0,1,0]
	v_pk_fma_f32 v[124:125], v[90:91], v[128:129], v[124:125] op_sel_hi:[0,1,1]
	v_pk_fma_f32 v[128:129], v[88:89], v[138:139], 0 op_sel_hi:[0,1,0]
	v_cvt_pk_f32_fp8_sdwa v[168:169], v168 src0_sel:WORD_1
	v_cvt_pk_f32_fp8_e32 v[182:183], v184
	v_cvt_pk_f32_fp8_e32 v[198:199], v200
	v_cvt_pk_f32_fp8_e32 v[214:215], v216
	v_pk_fma_f32 v[122:123], v[90:91], v[126:127], v[122:123] op_sel_hi:[0,1,1]
	v_pk_fma_f32 v[126:127], v[88:89], v[140:141], 0 op_sel_hi:[0,1,0]
	v_pk_fma_f32 v[140:141], v[88:89], v[154:155], 0 op_sel_hi:[0,1,0]
	v_pk_fma_f32 v[124:125], v[92:93], v[132:133], v[124:125] op_sel_hi:[0,1,1]
	v_pk_fma_f32 v[128:129], v[90:91], v[142:143], v[128:129] op_sel_hi:[0,1,1]
	v_pk_fma_f32 v[138:139], v[88:89], v[156:157], 0 op_sel_hi:[0,1,0]
	v_pk_fma_f32 v[154:155], v[88:89], v[172:173], 0 op_sel_hi:[0,1,0]
	v_pk_fma_f32 v[156:157], v[88:89], v[170:171], 0 op_sel_hi:[0,1,0]
	v_pk_fma_f32 v[170:171], v[88:89], v[188:189], 0 op_sel_hi:[0,1,0]
	v_pk_fma_f32 v[172:173], v[88:89], v[186:187], 0 op_sel_hi:[0,1,0]
	v_pk_fma_f32 v[186:187], v[88:89], v[204:205], 0 op_sel_hi:[0,1,0]
	v_pk_fma_f32 v[188:189], v[88:89], v[202:203], 0 op_sel_hi:[0,1,0]
	v_pk_fma_f32 v[202:203], v[88:89], v[220:221], 0 op_sel_hi:[0,1,0]
	v_pk_fma_f32 v[204:205], v[88:89], v[218:219], 0 op_sel_hi:[0,1,0]
	v_pk_fma_f32 v[218:219], v[88:89], v[236:237], 0 op_sel_hi:[0,1,0]
	v_pk_fma_f32 v[88:89], v[88:89], v[234:235], 0 op_sel_hi:[0,1,0]
	v_pk_fma_f32 v[122:123], v[92:93], v[130:131], v[122:123] op_sel_hi:[0,1,1]
	v_pk_fma_f32 v[126:127], v[90:91], v[144:145], v[126:127] op_sel_hi:[0,1,1]
	v_pk_fma_f32 v[130:131], v[90:91], v[158:159], v[140:141] op_sel_hi:[0,1,1]
	v_pk_fma_f32 v[124:125], v[94:95], v[136:137], v[124:125] op_sel_hi:[0,1,1]
	v_pk_fma_f32 v[128:129], v[92:93], v[146:147], v[128:129] op_sel_hi:[0,1,1]
	v_cvt_pk_f32_fp8_sdwa v[184:185], v184 src0_sel:WORD_1
	v_cvt_pk_f32_fp8_sdwa v[200:201], v200 src0_sel:WORD_1
	v_cvt_pk_f32_fp8_sdwa v[216:217], v216 src0_sel:WORD_1
	v_cvt_pk_f32_fp8_e32 v[230:231], v232
	v_cvt_pk_f32_fp8_sdwa v[232:233], v232 src0_sel:WORD_1
	s_waitcnt vmcnt(5)
	v_cvt_pk_f32_fp8_e32 v[246:247], v250
	v_pk_fma_f32 v[132:133], v[90:91], v[160:161], v[138:139] op_sel_hi:[0,1,1]
	v_pk_fma_f32 v[138:139], v[90:91], v[174:175], v[156:157] op_sel_hi:[0,1,1]
	v_pk_fma_f32 v[140:141], v[90:91], v[176:177], v[154:155] op_sel_hi:[0,1,1]
	v_pk_fma_f32 v[142:143], v[90:91], v[190:191], v[172:173] op_sel_hi:[0,1,1]
	v_pk_fma_f32 v[144:145], v[90:91], v[192:193], v[170:171] op_sel_hi:[0,1,1]
	v_pk_fma_f32 v[154:155], v[90:91], v[206:207], v[188:189] op_sel_hi:[0,1,1]
	v_pk_fma_f32 v[156:157], v[90:91], v[208:209], v[186:187] op_sel_hi:[0,1,1]
	v_pk_fma_f32 v[158:159], v[90:91], v[222:223], v[204:205] op_sel_hi:[0,1,1]
	v_pk_fma_f32 v[160:161], v[90:91], v[224:225], v[202:203] op_sel_hi:[0,1,1]
	v_pk_fma_f32 v[88:89], v[90:91], v[238:239], v[88:89] op_sel_hi:[0,1,1]
	v_pk_fma_f32 v[90:91], v[90:91], v[240:241], v[218:219] op_sel_hi:[0,1,1]
	v_pk_fma_f32 v[122:123], v[94:95], v[134:135], v[122:123] op_sel_hi:[0,1,1]
	v_pk_fma_f32 v[126:127], v[92:93], v[148:149], v[126:127] op_sel_hi:[0,1,1]
	v_pk_fma_f32 v[130:131], v[92:93], v[162:163], v[130:131] op_sel_hi:[0,1,1]
	v_pk_fma_f32 v[70:71], v[70:71], v[124:125], v[86:87]
	v_pk_fma_f32 v[86:87], v[94:95], v[150:151], v[128:129] op_sel_hi:[0,1,1]
	v_pk_fma_f32 v[132:133], v[92:93], v[164:165], v[132:133] op_sel_hi:[0,1,1]
	v_pk_fma_f32 v[134:135], v[92:93], v[180:181], v[140:141] op_sel_hi:[0,1,1]
	v_pk_fma_f32 v[136:137], v[92:93], v[178:179], v[138:139] op_sel_hi:[0,1,1]
	v_pk_fma_f32 v[138:139], v[92:93], v[196:197], v[144:145] op_sel_hi:[0,1,1]
	v_pk_fma_f32 v[140:141], v[92:93], v[194:195], v[142:143] op_sel_hi:[0,1,1]
	v_pk_fma_f32 v[142:143], v[92:93], v[212:213], v[156:157] op_sel_hi:[0,1,1]
	v_pk_fma_f32 v[144:145], v[92:93], v[210:211], v[154:155] op_sel_hi:[0,1,1]
	v_pk_fma_f32 v[146:147], v[92:93], v[228:229], v[160:161] op_sel_hi:[0,1,1]
	v_pk_fma_f32 v[148:149], v[92:93], v[226:227], v[158:159] op_sel_hi:[0,1,1]
	v_pk_fma_f32 v[90:91], v[92:93], v[244:245], v[90:91] op_sel_hi:[0,1,1]
	v_pk_fma_f32 v[88:89], v[92:93], v[242:243], v[88:89] op_sel_hi:[0,1,1]
	v_pk_fma_f32 v[68:69], v[68:69], v[122:123], v[120:121]
	v_pk_fma_f32 v[92:93], v[94:95], v[152:153], v[126:127] op_sel_hi:[0,1,1]
	v_pk_fma_f32 v[120:121], v[94:95], v[166:167], v[130:131] op_sel_hi:[0,1,1]
	s_waitcnt vmcnt(2)
	v_pk_fma_f32 v[72:73], v[72:73], v[86:87], v[98:99]
	v_cvt_pk_f32_fp8_sdwa v[250:251], v250 src0_sel:WORD_1
	v_pk_fma_f32 v[122:123], v[94:95], v[168:169], v[132:133] op_sel_hi:[0,1,1]
	v_pk_fma_f32 v[124:125], v[94:95], v[182:183], v[136:137] op_sel_hi:[0,1,1]
	v_pk_fma_f32 v[128:129], v[94:95], v[198:199], v[140:141] op_sel_hi:[0,1,1]
	v_pk_fma_f32 v[132:133], v[94:95], v[214:215], v[144:145] op_sel_hi:[0,1,1]
	v_mul_f32_e32 v59, v69, v69
	v_pk_fma_f32 v[74:75], v[74:75], v[92:93], v[100:101]
	v_pk_fma_f32 v[8:9], v[8:9], v[120:121], v[102:103]
	v_mul_f32_e32 v100, v73, v73
	v_pk_fma_f32 v[60:61], v[60:61], v[124:125], v[106:107]
	v_pk_fma_f32 v[64:65], v[64:65], v[128:129], v[110:111]
	s_waitcnt vmcnt(1)
	v_pk_fma_f32 v[76:77], v[76:77], v[132:133], v[114:115]
	v_fmac_f32_e32 v59, v68, v68
	v_mul_f32_e32 v101, v9, v9
	v_fmac_f32_e32 v100, v72, v72
	v_lshlrev_b32_e32 v248, 16, v96
	v_and_b32_e32 v249, 0xffff0000, v96
	v_pk_fma_f32 v[126:127], v[94:95], v[184:185], v[134:135] op_sel_hi:[0,1,1]
	v_pk_fma_f32 v[130:131], v[94:95], v[200:201], v[138:139] op_sel_hi:[0,1,1]
	v_pk_fma_f32 v[134:135], v[94:95], v[216:217], v[142:143] op_sel_hi:[0,1,1]
	v_pk_fma_f32 v[136:137], v[94:95], v[230:231], v[148:149] op_sel_hi:[0,1,1]
	v_pk_fma_f32 v[138:139], v[94:95], v[232:233], v[146:147] op_sel_hi:[0,1,1]
	v_pk_fma_f32 v[88:89], v[94:95], v[246:247], v[88:89] op_sel_hi:[0,1,1]
	v_pk_fma_f32 v[10:11], v[10:11], v[122:123], v[104:105]
	v_mul_f32_e32 v102, v61, v61
	v_mov_b32_e32 v86, v65
	v_mov_b32_e32 v87, v77
	v_fmac_f32_e32 v59, v70, v70
	v_fmac_f32_e32 v101, v8, v8
	v_fmac_f32_e32 v100, v74, v74
	v_pk_fma_f32 v[62:63], v[62:63], v[126:127], v[108:109]
	v_pk_fma_f32 v[66:67], v[66:67], v[130:131], v[112:113]
	v_pk_fma_f32 v[78:79], v[78:79], v[134:135], v[116:117]
	v_pk_fma_f32 v[6:7], v[6:7], v[138:139], v[84:85]
	v_pk_fma_f32 v[4:5], v[4:5], v[136:137], v[118:119]
	s_waitcnt vmcnt(0)
	v_pk_fma_f32 v[80:81], v[80:81], v[88:89], v[248:249]
	v_mov_b32_e32 v84, v64
	v_mov_b32_e32 v85, v76
	v_fmac_f32_e32 v102, v60, v60
	v_pk_mul_f32 v[86:87], v[86:87], v[86:87]
	v_fmac_f32_e32 v59, v71, v71
	v_fmac_f32_e32 v101, v10, v10
	v_fmac_f32_e32 v100, v75, v75
	v_lshlrev_b32_e32 v96, 16, v97
	v_and_b32_e32 v97, 0xffff0000, v97
	v_pk_fma_f32 v[90:91], v[94:95], v[250:251], v[90:91] op_sel_hi:[0,1,1]
	v_mov_b32_e32 v88, v66
	v_mov_b32_e32 v89, v78
	v_mov_b32_e32 v94, v5
	v_mov_b32_e32 v95, v81
	v_fmac_f32_e32 v102, v62, v62
	v_pk_fma_f32 v[84:85], v[84:85], v[84:85], v[86:87]
	v_fmac_f32_e32 v101, v11, v11
	v_add_f32_e32 v59, v59, v100
	v_pk_fma_f32 v[82:83], v[82:83], v[90:91], v[96:97]
	v_mov_b32_e32 v90, v67
	v_mov_b32_e32 v91, v79
	v_mov_b32_e32 v92, v4
	v_mov_b32_e32 v93, v80
	v_pk_mul_f32 v[94:95], v[94:95], v[94:95]
	v_fmac_f32_e32 v102, v63, v63
	v_pk_fma_f32 v[84:85], v[88:89], v[88:89], v[84:85]
	v_add_f32_e32 v59, v59, v101
	v_mov_b32_e32 v96, v6
	v_mov_b32_e32 v97, v82
	v_pk_fma_f32 v[86:87], v[92:93], v[92:93], v[94:95]
	v_pk_fma_f32 v[84:85], v[90:91], v[90:91], v[84:85]
	v_add_f32_e32 v59, v59, v102
	v_mov_b32_e32 v98, v7
	v_mov_b32_e32 v99, v83
	v_pk_fma_f32 v[86:87], v[96:97], v[96:97], v[86:87]
	v_add_f32_e32 v59, v59, v84
	v_pk_fma_f32 v[86:87], v[98:99], v[98:99], v[86:87]
	v_add_f32_e32 v59, v59, v85
	v_add_f32_e32 v59, v59, v86
	v_add_f32_e32 v59, v59, v87
	ds_bpermute_b32 v84, v42, v59
	s_waitcnt lgkmcnt(0)
	v_add_f32_e32 v59, v59, v84
	ds_bpermute_b32 v84, v43, v59
	s_waitcnt lgkmcnt(0)
	v_add_f32_e32 v59, v59, v84
	s_nop 1
	v_mov_b32_dpp v84, v59 row_ror:8 row_mask:0xf bank_mask:0xf
	s_waitcnt lgkmcnt(0)
	v_add_f32_e32 v59, v59, v84
	s_nop 1
	v_mov_b32_dpp v84, v59 row_ror:4 row_mask:0xf bank_mask:0xf
	s_waitcnt lgkmcnt(0)
	v_add_f32_e32 v59, v59, v84
	s_nop 1
	v_mov_b32_dpp v84, v59 quad_perm:[2,3,0,1] row_mask:0xf bank_mask:0xf
	s_waitcnt lgkmcnt(0)
	v_add_f32_e32 v59, v59, v84
	s_nop 1
	v_mov_b32_dpp v84, v59 quad_perm:[1,0,3,2] row_mask:0xf bank_mask:0xf
	s_waitcnt lgkmcnt(0)
	v_add_f32_e32 v59, v59, v84
	v_fmamk_f32 v59, v59, 0x3a000000, v58
	v_mul_f32_e32 v84, 0x4b800000, v59
	v_cmp_gt_f32_e32 vcc, s5, v59
	s_nop 1
	v_cndmask_b32_e32 v59, v59, v84, vcc
	v_rsq_f32_e32 v59, v59
	s_nop 0
	v_mul_f32_e32 v84, 0x45800000, v59
	v_cndmask_b32_e32 v84, v59, v84, vcc
	v_pk_mul_f32 v[68:69], v[68:69], v[84:85] op_sel_hi:[1,0]
	v_pk_mul_f32 v[70:71], v[70:71], v[84:85] op_sel_hi:[1,0]
	v_pk_mul_f32 v[0:1], v[0:1], v[68:69]
	v_pk_mul_f32 v[2:3], v[2:3], v[70:71]
	global_store_dwordx4 v[38:39], v[0:3], off offset:-4096
	global_load_dwordx4 v[0:3], v[12:13], off offset:1024
	v_pk_mul_f32 v[68:69], v[74:75], v[84:85] op_sel_hi:[1,0]
	v_pk_mul_f32 v[70:71], v[72:73], v[84:85] op_sel_hi:[1,0]
	v_pk_mul_f32 v[10:11], v[10:11], v[84:85] op_sel_hi:[1,0]
	v_pk_mul_f32 v[8:9], v[8:9], v[84:85] op_sel_hi:[1,0]
	v_pk_mul_f32 v[6:7], v[6:7], v[84:85] op_sel_hi:[1,0]
	v_pk_mul_f32 v[4:5], v[4:5], v[84:85] op_sel_hi:[1,0]
	s_waitcnt vmcnt(0)
	v_pk_mul_f32 v[0:1], v[0:1], v[70:71]
	v_pk_mul_f32 v[2:3], v[2:3], v[68:69]
	global_store_dwordx4 v[38:39], v[0:3], off offset:-3072
	global_load_dwordx4 v[0:3], v[12:13], off offset:2048
	s_waitcnt vmcnt(0)
	v_pk_mul_f32 v[0:1], v[0:1], v[8:9]
	v_pk_mul_f32 v[2:3], v[2:3], v[10:11]
	global_store_dwordx4 v[38:39], v[0:3], off offset:-2048
	global_load_dwordx4 v[0:3], v[12:13], off offset:3072
	v_pk_mul_f32 v[8:9], v[62:63], v[84:85] op_sel_hi:[1,0]
	v_pk_mul_f32 v[10:11], v[60:61], v[84:85] op_sel_hi:[1,0]
	s_waitcnt vmcnt(0)
	v_pk_mul_f32 v[2:3], v[2:3], v[8:9]
	v_pk_mul_f32 v[0:1], v[0:1], v[10:11]
	global_store_dwordx4 v[38:39], v[0:3], off offset:-1024
	global_load_dwordx4 v[0:3], v[30:31], off
	v_pk_mul_f32 v[8:9], v[66:67], v[84:85] op_sel_hi:[1,0]
	v_pk_mul_f32 v[10:11], v[64:65], v[84:85] op_sel_hi:[1,0]
	s_waitcnt vmcnt(0)
	v_pk_mul_f32 v[2:3], v[2:3], v[8:9]
	v_pk_mul_f32 v[0:1], v[0:1], v[10:11]
	global_store_dwordx4 v[38:39], v[0:3], off
	global_load_dwordx4 v[0:3], v[32:33], off
	v_pk_mul_f32 v[8:9], v[78:79], v[84:85] op_sel_hi:[1,0]
	v_pk_mul_f32 v[10:11], v[76:77], v[84:85] op_sel_hi:[1,0]
	s_waitcnt vmcnt(0)
	v_pk_mul_f32 v[2:3], v[2:3], v[8:9]
	v_pk_mul_f32 v[0:1], v[0:1], v[10:11]
	global_store_dwordx4 v[38:39], v[0:3], off offset:1024
	global_load_dwordx4 v[0:3], v[34:35], off
	s_waitcnt vmcnt(0)
	v_pk_mul_f32 v[0:1], v[0:1], v[4:5]
	v_pk_mul_f32 v[2:3], v[2:3], v[6:7]
	global_store_dwordx4 v[38:39], v[0:3], off offset:2048
	global_load_dwordx4 v[0:3], v[36:37], off
	v_pk_mul_f32 v[4:5], v[82:83], v[84:85] op_sel_hi:[1,0]
	v_pk_mul_f32 v[6:7], v[80:81], v[84:85] op_sel_hi:[1,0]
	s_waitcnt vmcnt(0)
	v_pk_mul_f32 v[2:3], v[2:3], v[4:5]
	v_pk_mul_f32 v[0:1], v[0:1], v[6:7]
	global_store_dwordx4 v[38:39], v[0:3], off offset:3072
	v_lshl_add_u64 v[38:39], v[38:39], 0, s[10:11]
	s_cbranch_scc1 .LBB0_1168
